# v61 + norm2: non-temporal hint on the once-read y0/y1 row loads
# baseline (speedup 1.0000x reference)
; __device__ __forceinline__ unsigned pk2(float lo, float hi) { f32x2_cv_ v = {lo, hi}; return __builtin_bit_cast(unsigned, __builtin_convertvector(v, bf16x2_cv_)); }
; __device__ __forceinline__ void phase_norm2(Frame& F, int l, float ysc) {
;     ...
;     for (int row0 = 2 * F.gw(); row0 < T; row0 += 2 * F.ngw()) {
;         u32x4 hw[2][2], ya[2][2], yb[2][2];
; #pragma unroll
;         for (int q = 0; q < 2; ++q) { const u32x4* xr = (const u32x4*)(HB + (size_t)(row0 + q) * DM) + F.lane; const u32x4* y0 = (const u32x4*)(Y + (size_t)(row0 + q) * 2 * DM) + F.lane; const u32x4* y1 = y0 + DM / 8;
; #pragma unroll
;             for (int j = 0; j < 2; ++j) { hw[q][j] = xr[64 * j]; ya[q][j] = y0[64 * j]; yb[q][j] = y1[64 * j]; } }
; #pragma unroll
;         for (int q = 0; q < 2; ++q) { float s = 0.f; u32x4* xr = (u32x4*)(HB + (size_t)(row0 + q) * DM) + F.lane;
; #pragma unroll
;             for (int j = 0; j < 2; ++j) { float h[8], a[8], b[8]; unpack8(hw[q][j], h); unpack8(ya[q][j], a); unpack8(yb[q][j], b);
; #pragma unroll
;                 for (int i = 0; i < 8; ++i) h[i] += ysc * (a[i] + b[i]);
;                 const u32x4 o = (u32x4){pk2(h[0], h[1]), pk2(h[2], h[3]), pk2(h[4], h[5]), pk2(h[6], h[7])}; xr[64 * j] = o;
;                 unpack8(o, h);
; #pragma unroll
;                 for (int i = 0; i < 8; i += 4) s += (h[i] * h[i] + h[i + 1] * h[i + 1]) + (h[i + 2] * h[i + 2] + h[i + 3] * h[i + 3]); }
;             s = wave_sum(s);
;             if (F.lane == 0) RS[row0 + q] = 1.0f / sqrtf(s * (1.f / DM) + EPS); }
.LBB0_1421:
	v_lshl_add_u64 v[42:43], s[74:75], 0, v[40:41]
	v_add_co_u32_e32 v44, vcc, 0xee00000, v42
	v_lshl_add_u64 v[2:3], s[74:75], 0, v[38:39]
	s_nop 0
	v_addc_co_u32_e32 v45, vcc, 0, v43, vcc
	global_load_dwordx4 v[46:49], v[44:45], off
	v_add_co_u32_e32 v4, vcc, 0x15200000, v2
	s_mov_b32 s3, 0x15201000
	s_nop 0
	v_addc_co_u32_e32 v5, vcc, 0, v3, vcc
	global_load_dwordx4 v[50:53], v[4:5], off nt
	global_load_dwordx4 v[54:57], v[4:5], off offset:2048 nt
	global_load_dwordx4 v[26:29], v[44:45], off offset:1024
	global_load_dwordx4 v[34:37], v[4:5], off offset:1024 nt
	global_load_dwordx4 v[30:33], v[4:5], off offset:3072 nt
	global_load_dwordx4 v[14:17], v[44:45], off offset:2048
	v_add_co_u32_e32 v10, vcc, s3, v2
	s_nop 1
	v_addc_co_u32_e32 v11, vcc, 0, v3, vcc
	global_load_dwordx4 v[22:25], v[10:11], off nt
	global_load_dwordx4 v[18:21], v[10:11], off offset:2048 nt
	global_load_dwordx4 v[2:5], v[44:45], off offset:3072
	global_load_dwordx4 v[6:9], v[10:11], off offset:1024 nt
	s_nop 0
	global_load_dwordx4 v[10:13], v[10:11], off offset:3072 nt
	s_waitcnt vmcnt(6)
	v_lshlrev_b32_e32 v58, 16, v46
	v_lshlrev_b32_e32 v60, 16, v50
	v_and_b32_e32 v61, 0xffff0000, v50
	v_lshlrev_b32_e32 v62, 16, v54
	v_and_b32_e32 v63, 0xffff0000, v54
	v_and_b32_e32 v59, 0xffff0000, v46
	v_pk_add_f32 v[60:61], v[60:61], v[62:63]
	v_lshlrev_b32_e32 v50, 16, v51
	v_and_b32_e32 v51, 0xffff0000, v51
	v_lshlrev_b32_e32 v54, 16, v55
	v_and_b32_e32 v55, 0xffff0000, v55
	v_pk_add_f32 v[58:59], v[60:61], v[58:59]
	v_lshlrev_b32_e32 v46, 16, v47
	v_and_b32_e32 v47, 0xffff0000, v47
	v_pk_add_f32 v[50:51], v[50:51], v[54:55]
	v_lshlrev_b32_e32 v54, 16, v52
	v_and_b32_e32 v55, 0xffff0000, v52
	v_lshlrev_b32_e32 v60, 16, v56
	v_and_b32_e32 v61, 0xffff0000, v56
	v_pk_add_f32 v[50:51], v[50:51], v[46:47]
	v_lshlrev_b32_e32 v46, 16, v48
	v_and_b32_e32 v47, 0xffff0000, v48
	v_pk_add_f32 v[54:55], v[54:55], v[60:61]
	v_lshlrev_b32_e32 v48, 16, v53
	v_pk_add_f32 v[54:55], v[54:55], v[46:47]
	v_lshlrev_b32_e32 v46, 16, v49
	v_and_b32_e32 v47, 0xffff0000, v49
	v_and_b32_e32 v49, 0xffff0000, v53
	v_lshlrev_b32_e32 v52, 16, v57
	v_and_b32_e32 v53, 0xffff0000, v57
	v_pk_add_f32 v[48:49], v[48:49], v[52:53]
	s_nop 0
	v_pk_add_f32 v[52:53], v[48:49], v[46:47]
	v_cvt_pk_bf16_f32 v46, v58, v59
	v_cvt_pk_bf16_f32 v47, v50, v51
	v_cvt_pk_bf16_f32 v48, v54, v55
	v_cvt_pk_bf16_f32 v49, v52, v53
	global_store_dwordx4 v[44:45], v[46:49], off
	v_lshlrev_b32_e32 v0, 16, v46
	v_lshlrev_b32_e32 v50, 16, v47
	v_and_b32_e32 v46, 0xffff0000, v46
	v_and_b32_e32 v47, 0xffff0000, v47
	v_mul_f32_e32 v46, v46, v46
	v_fmac_f32_e32 v46, v0, v0
	v_mul_f32_e32 v0, v47, v47
	v_lshlrev_b32_e32 v51, 16, v48
	v_and_b32_e32 v48, 0xffff0000, v48
	v_lshlrev_b32_e32 v52, 16, v49
	v_and_b32_e32 v49, 0xffff0000, v49
	v_fmac_f32_e32 v0, v50, v50
	v_add_f32_e32 v0, v46, v0
	v_mul_f32_e32 v46, v48, v48
	v_mul_f32_e32 v47, v49, v49
	v_fmac_f32_e32 v46, v51, v51
	v_fmac_f32_e32 v47, v52, v52
	v_add_f32_e32 v46, v46, v47
	v_lshlrev_b32_e32 v48, 16, v34
	v_and_b32_e32 v49, 0xffff0000, v34
	v_lshlrev_b32_e32 v50, 16, v30
	v_and_b32_e32 v51, 0xffff0000, v30
	v_add_f32_e32 v0, v0, v46
	v_lshlrev_b32_e32 v46, 16, v26
	v_and_b32_e32 v47, 0xffff0000, v26
	v_pk_add_f32 v[48:49], v[48:49], v[50:51]
	v_lshlrev_b32_e32 v34, 16, v35
	v_and_b32_e32 v35, 0xffff0000, v35
	v_lshlrev_b32_e32 v30, 16, v31
	v_and_b32_e32 v31, 0xffff0000, v31
	v_pk_add_f32 v[46:47], v[48:49], v[46:47]
	v_lshlrev_b32_e32 v26, 16, v27
	v_and_b32_e32 v27, 0xffff0000, v27
	v_pk_add_f32 v[30:31], v[34:35], v[30:31]
	v_lshlrev_b32_e32 v34, 16, v36
	v_and_b32_e32 v35, 0xffff0000, v36
	v_lshlrev_b32_e32 v48, 16, v32
	v_and_b32_e32 v49, 0xffff0000, v32
	v_pk_add_f32 v[30:31], v[30:31], v[26:27]
	v_lshlrev_b32_e32 v26, 16, v28
	v_and_b32_e32 v27, 0xffff0000, v28
	v_pk_add_f32 v[34:35], v[34:35], v[48:49]
	v_lshlrev_b32_e32 v28, 16, v37
	v_pk_add_f32 v[34:35], v[34:35], v[26:27]
	v_lshlrev_b32_e32 v26, 16, v29
	v_and_b32_e32 v27, 0xffff0000, v29
	v_and_b32_e32 v29, 0xffff0000, v37
	v_lshlrev_b32_e32 v32, 16, v33
	v_and_b32_e32 v33, 0xffff0000, v33
	v_pk_add_f32 v[28:29], v[28:29], v[32:33]
	s_nop 0
	v_pk_add_f32 v[32:33], v[28:29], v[26:27]
	v_cvt_pk_bf16_f32 v26, v46, v47
	v_cvt_pk_bf16_f32 v27, v30, v31
	v_cvt_pk_bf16_f32 v28, v34, v35
	v_cvt_pk_bf16_f32 v29, v32, v33
	global_store_dwordx4 v[44:45], v[26:29], off offset:1024
	v_lshlrev_b32_e32 v30, 16, v26
	v_lshlrev_b32_e32 v31, 16, v27
	v_and_b32_e32 v26, 0xffff0000, v26
	v_and_b32_e32 v27, 0xffff0000, v27
	v_mul_f32_e32 v26, v26, v26
	v_mul_f32_e32 v27, v27, v27
	v_fmac_f32_e32 v26, v30, v30
	v_fmac_f32_e32 v27, v31, v31
	v_lshlrev_b32_e32 v32, 16, v28
	v_and_b32_e32 v28, 0xffff0000, v28
	v_lshlrev_b32_e32 v33, 16, v29
	v_and_b32_e32 v29, 0xffff0000, v29
	v_add_f32_e32 v26, v26, v27
	v_add_f32_e32 v0, v0, v26
	v_mul_f32_e32 v26, v28, v28
	v_mul_f32_e32 v27, v29, v29
	v_fmac_f32_e32 v26, v32, v32
	v_fmac_f32_e32 v27, v33, v33
	v_add_f32_e32 v26, v26, v27
	v_add_f32_e32 v0, v26, v0
	s_nop 1
	v_add_f32_dpp v0, v0, v0 quad_perm:[1,0,3,2] row_mask:0xf bank_mask:0xf bound_ctrl:1
	s_nop 1
	v_add_f32_dpp v0, v0, v0 quad_perm:[2,3,0,1] row_mask:0xf bank_mask:0xf bound_ctrl:1
	s_nop 1
	v_add_f32_dpp v0, v0, v0 row_half_mirror row_mask:0xf bank_mask:0xf bound_ctrl:1
	s_nop 1
	v_add_f32_dpp v0, v0, v0 row_mirror row_mask:0xf bank_mask:0xf bound_ctrl:1
	s_nop 0
	v_readlane_b32 s12, v0, 0
	v_readlane_b32 s3, v0, 16
	v_readlane_b32 s13, v0, 32
	v_readlane_b32 s6, v0, 48
	s_and_saveexec_b64 s[16:17], s[10:11]
	s_cbranch_execz .LBB0_1423
	v_mov_b32_e32 v26, s3
	v_mov_b32_e32 v27, s6
	v_pk_add_f32 v[26:27], s[12:13], v[26:27]
	s_mov_b32 s3, 0xf800000
	v_add_f32_e32 v0, v26, v27
	v_fmamk_f32 v0, v0, 0x3a800000, v236
	v_mul_f32_e32 v26, 0x4f800000, v0
	v_cmp_gt_f32_e32 vcc, s3, v0
	s_add_u32 s3, s74, s14
	s_nop 0
	v_cndmask_b32_e32 v0, v0, v26, vcc
	v_sqrt_f32_e32 v26, v0
	s_nop 0
	v_add_u32_e32 v27, -1, v26
	v_fma_f32 v28, -v27, v26, v0
	v_cmp_ge_f32_e64 s[12:13], 0, v28
	v_add_u32_e32 v28, 1, v26
	s_nop 0
	v_cndmask_b32_e64 v27, v26, v27, s[12:13]
	v_fma_f32 v26, -v28, v26, v0
	v_cmp_lt_f32_e64 s[12:13], 0, v26
	s_nop 1
	v_cndmask_b32_e64 v26, v27, v28, s[12:13]
	v_mul_f32_e32 v27, 0x37800000, v26
	v_cndmask_b32_e32 v26, v26, v27, vcc
	v_cmp_class_f32_e32 vcc, v0, v251
	s_nop 1
	v_cndmask_b32_e32 v0, v26, v0, vcc
	v_div_scale_f32 v26, s[6:7], v0, v0, 1.0
	v_rcp_f32_e32 v27, v26
	s_addc_u32 s6, s75, s15
	v_fma_f32 v28, -v26, v27, 1.0
	v_fmac_f32_e32 v27, v28, v27
	v_div_scale_f32 v28, vcc, 1.0, v0, 1.0
	v_mul_f32_e32 v29, v28, v27
	v_fma_f32 v30, -v26, v29, v28
	v_fmac_f32_e32 v29, v30, v27
	v_fma_f32 v26, -v26, v29, v28
	v_div_fmas_f32 v26, v26, v27, v29
	v_div_fixup_f32 v0, v26, v0, 1.0
	v_mov_b32_e32 v26, s3
	v_add_co_u32_e32 v26, vcc, 0x500000, v26
	v_mov_b32_e32 v27, s6
	s_nop 0
	v_addc_co_u32_e32 v27, vcc, 0, v27, vcc
	global_store_dword v[26:27], v0, off
